# plus non-temporal stores for the bf16 residual stream (xb) in N1/N2 and the final f32 output
# baseline (speedup 1.0000x reference)
; DI const float* inp(kptr_t k, int i) { return (const float*)k[i]; }
; DI void phase_n1(Frame& F, int l) {
;     ...
;         const float* mb = mod + (size_t)((blk * 16) / SEQ) * NMOD * D;
;         f32x4 gpm[4], gtm[4]; ModP mp;
; #pragma unroll
;         for (int j = 0; j < 4; ++j) { const int o = 4 * F.lane + 256 * j; gpm[j] = *(const f32x4*)(inp(KA, I_GPOSTMIX) + l * D + o); gtm[j] = *(const f32x4*)(mb + 2 * D + o); }
;         load_modp(mp, inp(KA, I_GPREFFN) + l * D, mb + 4 * D, mb + 3 * D, F.lane);
; #pragma unroll
;         for (int rr = 0; rr < 2; ++rr) { const int r = blk * 16 + F.wave * 2 + rr;
;             f32x4 (&yv)[4] = yv2[rr]; f32x4 (&xv)[4] = xv2[rr];
;             const float rstd_y = rsqrtf(sumsq(yv, F.lane) * (1.0f / D) + RMS_EPS);
.LBB0_1040:
	s_ashr_i32 s0, s30, 31
	s_lshr_b32 s0, s0, 25
	s_add_i32 s0, s30, s0
	s_ashr_i32 s0, s0, 7
	s_mul_i32 s0, s0, 6
	s_ashr_i32 s1, s0, 31
	s_lshl_b64 s[0:1], s[0:1], 12
	s_add_u32 s0, s31, s0
	s_addc_u32 s1, s33, s1
	v_lshl_add_u64 v[34:35], s[0:1], 0, v[110:111]
	s_movk_i32 s0, 0x4000
	v_add_co_u32_e32 v36, vcc, s0, v34
	s_mov_b64 s[0:1], 0x4000
	s_nop 0
	v_addc_co_u32_e32 v37, vcc, 0, v35, vcc
	global_load_dwordx4 v[112:115], v[36:37], off
	v_lshl_add_u64 v[36:37], v[34:35], 0, s[0:1]
	global_load_dwordx4 v[140:143], v[36:37], off offset:1024
	global_load_dwordx4 v[156:159], v[36:37], off offset:2048
	s_load_dwordx4 s[16:19], s[20:21], 0x30
	s_waitcnt vmcnt(0)
	v_lshlrev_b32_e32 v169, 16, v23
	v_lshlrev_b32_e32 v168, 16, v22
	v_and_b32_e32 v171, 0xffff0000, v23
	v_and_b32_e32 v170, 0xffff0000, v22
	s_waitcnt lgkmcnt(0)
	s_add_u32 s0, s16, s24
	s_addc_u32 s1, s17, s25
	v_lshl_add_u64 v[22:23], s[0:1], 0, v[110:111]
	s_movk_i32 s0, 0x3000
	v_lshlrev_b32_e32 v172, 16, v20
	v_and_b32_e32 v173, 0xffff0000, v20
	v_add_co_u32_e32 v20, vcc, s0, v34
	v_lshlrev_b32_e32 v174, 16, v21
	v_and_b32_e32 v175, 0xffff0000, v21
	global_load_dwordx4 v[70:73], v[22:23], off
	global_load_dwordx4 v[94:97], v[22:23], off offset:1024
	v_addc_co_u32_e32 v21, vcc, 0, v35, vcc
	global_load_dwordx4 v[74:77], v[20:21], off offset:-4096
	v_and_b32_e32 v167, 0xffff0000, v25
	v_lshlrev_b32_e32 v166, 16, v25
	v_lshlrev_b32_e32 v177, 16, v18
	global_load_dwordx4 v[160:163], v[36:37], off offset:3072
	v_and_b32_e32 v179, 0xffff0000, v18
	v_mul_f32_e32 v18, v167, v167
	s_mov_b64 s[0:1], 0x2000
	v_lshlrev_b32_e32 v180, 16, v19
	v_and_b32_e32 v181, 0xffff0000, v19
	v_pk_fma_f32 v[144:145], v[166:167], v[166:167], v[18:19] op_sel_hi:[1,1,0]
	v_lshl_add_u64 v[18:19], v[34:35], 0, s[0:1]
	global_load_dwordx4 v[90:93], v[18:19], off offset:1024
	v_lshlrev_b32_e32 v164, 16, v24
	v_and_b32_e32 v165, 0xffff0000, v24
	v_pk_mul_f32 v[24:25], v[170:171], v[170:171]
	s_mov_b64 s[0:1], 0x3000
	v_lshlrev_b32_e32 v128, 16, v28
	v_and_b32_e32 v129, 0xffff0000, v28
	v_lshlrev_b32_e32 v130, 16, v29
	v_and_b32_e32 v131, 0xffff0000, v29
	v_lshlrev_b32_e32 v121, 16, v26
	v_and_b32_e32 v119, 0xffff0000, v26
	v_lshlrev_b32_e32 v122, 16, v27
	v_and_b32_e32 v123, 0xffff0000, v27
	v_pk_fma_f32 v[182:183], v[168:169], v[168:169], v[24:25]
	v_lshl_add_u64 v[24:25], v[34:35], 0, s[0:1]
	global_load_dwordx4 v[82:85], v[18:19], off offset:2048
	global_load_dwordx4 v[66:69], v[18:19], off offset:3072
	global_load_dwordx4 v[46:49], v[20:21], off
	global_load_dwordx4 v[86:89], v[22:23], off offset:2048
	global_load_dwordx4 v[34:37], v[24:25], off offset:1024
	global_load_dwordx4 v[26:29], v[24:25], off offset:2048
	s_nop 0
	global_load_dwordx4 v[18:21], v[24:25], off offset:3072
	global_load_dwordx4 v[78:81], v[22:23], off offset:3072
	s_add_u32 s0, s18, s24
	s_addc_u32 s1, s19, s25
	v_lshl_add_u64 v[22:23], s[0:1], 0, v[110:111]
	v_lshlrev_b32_e32 v136, 16, v32
	v_and_b32_e32 v137, 0xffff0000, v32
	v_lshlrev_b32_e32 v138, 16, v33
	v_and_b32_e32 v139, 0xffff0000, v33
	v_lshlrev_b32_e32 v133, 16, v31
	v_lshlrev_b32_e32 v132, 16, v30
	v_and_b32_e32 v135, 0xffff0000, v31
	v_and_b32_e32 v134, 0xffff0000, v30
	global_load_dwordx4 v[54:57], v[22:23], off
	global_load_dwordx4 v[42:45], v[22:23], off offset:1024
	global_load_dwordx4 v[30:33], v[22:23], off offset:2048
	s_nop 0
	global_load_dwordx4 v[22:25], v[22:23], off offset:3072
	v_mul_f32_e32 v118, v165, v165
	v_mul_f32_e32 v109, v179, v179
	v_mul_f32_e32 v120, v180, v180
	v_mul_f32_e32 v155, v181, v181
	v_mov_b32_e32 v178, v177
	v_pk_add_f32 v[124:125], v[114:115], 1.0 op_sel_hi:[1,0]
	v_pk_add_f32 v[116:117], v[140:141], 1.0 op_sel_hi:[1,0]
	v_pk_fma_f32 v[140:141], v[164:165], v[164:165], v[118:119] op_sel_hi:[1,1,0]
	v_pk_add_f32 v[114:115], v[142:143], 1.0 op_sel_hi:[1,0]
	v_mov_b32_e32 v176, v140
	v_mov_b32_e32 v142, v144
	v_mov_b32_e32 v143, v177
	v_pk_add_f32 v[140:141], v[140:141], v[144:145]
	v_pk_mul_f32 v[142:143], v[176:177], v[142:143]
	v_mul_f32_e32 v118, v173, v173
	v_mov_b32_e32 v141, v143
	v_pk_add_f32 v[142:143], v[182:183], v[182:183] op_sel:[0,1] op_sel_hi:[1,0]
	v_mov_b32_e32 v176, 0x358637bd
	v_mov_b32_e32 v143, v109
	v_pk_add_f32 v[140:141], v[140:141], v[142:143]
	v_pk_fma_f32 v[142:143], v[172:173], v[172:173], v[118:119] op_sel_hi:[1,1,0]
	v_mul_f32_e32 v118, v175, v175
	v_pk_fma_f32 v[144:145], v[174:175], v[174:175], v[118:119] op_sel_hi:[1,1,0]
	v_mov_b32_e32 v143, v120
	v_mov_b32_e32 v145, v155
	v_pk_add_f32 v[142:143], v[142:143], v[144:145]
	v_mov_b32_e32 v118, v1
	v_pk_add_f32 v[140:141], v[140:141], v[142:143]
	v_mov_b32_e32 v182, 0x3a800000
	v_add_f32_e32 v109, v140, v141
	v_pk_add_f32 v[126:127], v[112:113], 1.0 op_sel_hi:[1,0]
	v_pk_add_f32 v[112:113], v[158:159], 1.0 op_sel_hi:[1,0]
	v_add_f32_dpp v109, v109, v109 row_shr:1 row_mask:0xf bank_mask:0xf bound_ctrl:1
	v_pk_add_f32 v[144:145], v[156:157], 1.0 op_sel_hi:[1,0]
	s_waitcnt vmcnt(13)
; DI unsigned pk2(float lo, float hi) { f32x2 v = {lo, hi}; bf16x2v r = __builtin_convertvector(v, bf16x2v); return __builtin_bit_cast(unsigned, r); }
; DI void phase_n1(Frame& F, int l) {
;     ...
;         for (int rr = 0; rr < 2; ++rr) { const int r = blk * 16 + F.wave * 2 + rr;
;             f32x4 (&yv)[4] = yv2[rr]; f32x4 (&xv)[4] = xv2[rr];
;             const float rstd_y = rsqrtf(sumsq(yv, F.lane) * (1.0f / D) + RMS_EPS);
; #pragma unroll
;             for (int j = 0; j < 4; ++j) { const int o = 4 * F.lane + 256 * j; const f32x4 gv = gpm[j], gt = gtm[j];
;                 xv[j] = xv[j] + gt * (yv[j] * rstd_y * gv); u32x2 w; w.x = pk2(xv[j][0], xv[j][1]); w.y = pk2(xv[j][2], xv[j][3]); *(u32x2*)(xb + (size_t)r * D + o) = w; }
;             const float rstd_x = rsqrtf(sumsq(xv, F.lane) * (1.0f / D) + RMS_EPS);
;             mod_norm_store8(xv, rstd_x, mp, h8 + (size_t)r * D, F.lane, hv[rr]); }
	v_pk_add_f32 v[142:143], v[160:161], 1.0 op_sel_hi:[1,0]
	v_add_f32_dpp v109, v109, v109 row_shr:2 row_mask:0xf bank_mask:0xf bound_ctrl:1
	v_pk_add_f32 v[140:141], v[162:163], 1.0 op_sel_hi:[1,0]
	v_mov_b32_e32 v155, v1
	v_add_f32_dpp v109, v109, v109 row_shr:4 row_mask:0xf bank_mask:0xf bound_ctrl:1
	s_nop 1
	v_add_f32_dpp v109, v109, v109 row_shr:8 row_mask:0xf bank_mask:0xf bound_ctrl:1
	s_nop 1
	v_mov_b32_dpp v118, v109 row_bcast:15 row_mask:0xa bank_mask:0xf
	v_add_f32_e32 v109, v109, v118
	v_mov_b32_e32 v118, v1
	s_nop 1
	v_mov_b32_dpp v118, v109 row_bcast:31 row_mask:0xc bank_mask:0xf
	v_add_f32_e32 v109, v109, v118
	s_nop 0
	v_readlane_b32 s0, v109, 63
	s_nop 1
	v_fma_f32 v109, s0, v182, v176
	v_mul_f32_e32 v118, 0x4b800000, v109
	v_cmp_gt_f32_e32 vcc, s51, v109
	s_nop 1
	v_cndmask_b32_e32 v109, v109, v118, vcc
	v_rsq_f32_e32 v109, v109
	s_nop 0
	v_mul_f32_e32 v118, 0x45800000, v109
	v_cndmask_b32_e32 v118, v109, v118, vcc
	v_pk_mul_f32 v[156:157], v[118:119], v[166:167] op_sel_hi:[0,1]
	v_pk_mul_f32 v[158:159], v[118:119], v[164:165] op_sel_hi:[0,1]
	v_pk_mul_f32 v[158:159], v[70:71], v[158:159]
	v_pk_mul_f32 v[156:157], v[72:73], v[156:157]
	v_pk_fma_f32 v[62:63], v[74:75], v[158:159], v[62:63]
	v_pk_fma_f32 v[64:65], v[76:77], v[156:157], v[64:65]
	v_cvt_pk_bf16_f32 v156, v62, v63
	v_cvt_pk_bf16_f32 v157, v64, v65
	v_lshl_add_u64 v[158:159], v[100:101], 0, s[28:29]
	global_store_dwordx2 v[158:159], v[156:157], off nt
	v_mov_b32_e32 v156, v169
	v_mov_b32_e32 v157, v171
	v_mov_b32_e32 v169, v170
	v_pk_mul_f32 v[156:157], v[118:119], v[156:157] op_sel_hi:[0,1]
	v_pk_mul_f32 v[160:161], v[118:119], v[168:169] op_sel_hi:[0,1]
	v_pk_mul_f32 v[160:161], v[94:95], v[160:161]
	v_pk_mul_f32 v[156:157], v[96:97], v[156:157]
	s_waitcnt vmcnt(13)
	v_pk_fma_f32 v[58:59], v[90:91], v[160:161], v[58:59]
	v_pk_fma_f32 v[60:61], v[92:93], v[156:157], v[60:61]
	v_cvt_pk_bf16_f32 v156, v58, v59
	v_cvt_pk_bf16_f32 v157, v60, v61
	global_store_dwordx2 v[158:159], v[156:157], off offset:512 nt
	v_pk_mul_f32 v[156:157], v[118:119], v[174:175] op_sel_hi:[0,1]
	s_waitcnt vmcnt(10)
	v_pk_mul_f32 v[156:157], v[88:89], v[156:157]
	v_pk_mul_f32 v[162:163], v[118:119], v[178:179] op_sel_hi:[0,1]
	v_pk_fma_f32 v[156:157], v[84:85], v[156:157], v[52:53]
	v_pk_mul_f32 v[52:53], v[118:119], v[180:181] op_sel_hi:[0,1]
	s_waitcnt vmcnt(6)
	v_pk_mul_f32 v[162:163], v[78:79], v[162:163]
	v_pk_mul_f32 v[52:53], v[80:81], v[52:53]
	v_pk_fma_f32 v[162:163], v[66:67], v[162:163], v[38:39]
	v_pk_fma_f32 v[164:165], v[68:69], v[52:53], v[40:41]
	v_pk_mul_f32 v[38:39], v[64:65], v[64:65]
	v_pk_mul_f32 v[40:41], v[62:63], v[62:63]
	v_pk_mul_f32 v[160:161], v[118:119], v[172:173] op_sel_hi:[0,1]
	v_pk_mov_b32 v[52:53], v[40:41], v[38:39] op_sel:[1,0]
	v_mov_b32_e32 v41, v39
	v_pk_mul_f32 v[160:161], v[86:87], v[160:161]
	v_pk_add_f32 v[38:39], v[52:53], v[40:41]
	v_pk_fma_f32 v[160:161], v[82:83], v[160:161], v[50:51]
	v_pk_add_f32 v[38:39], v[38:39], v[38:39] op_sel_hi:[0,1]
	v_pk_mul_f32 v[40:41], v[60:61], v[60:61]
	v_pk_mul_f32 v[52:53], v[58:59], v[58:59]
	v_mul_f32_e32 v38, v160, v160
	v_pk_mov_b32 v[166:167], v[52:53], v[40:41] op_sel:[1,0]
	v_mov_b32_e32 v53, v41
	v_pk_add_f32 v[40:41], v[166:167], v[52:53]
	v_pk_fma_f32 v[52:53], v[160:161], v[160:161], v[38:39] op_sel_hi:[1,1,0]
	v_mul_f32_e32 v38, v156, v156
	v_pk_add_f32 v[40:41], v[40:41], v[40:41] op_sel_hi:[0,1]
	v_pk_fma_f32 v[166:167], v[156:157], v[156:157], v[38:39] op_sel_hi:[1,1,0]
	v_mul_f32_e32 v52, v162, v162
	v_mul_f32_e32 v166, v163, v163
	v_mul_f32_e32 v38, v164, v164
	v_mul_f32_e32 v40, v165, v165
	v_pk_add_f32 v[52:53], v[52:53], v[166:167]
	v_pk_add_f32 v[38:39], v[38:39], v[40:41]
	v_cvt_pk_bf16_f32 v50, v160, v161
	v_pk_add_f32 v[38:39], v[52:53], v[38:39]
	v_cvt_pk_bf16_f32 v51, v156, v157
	v_add_f32_e32 v38, v38, v39
	v_mov_b32_e32 v39, v1
	global_store_dwordx2 v[158:159], v[50:51], off offset:1024 nt
	v_add_f32_dpp v38, v38, v38 row_shr:1 row_mask:0xf bank_mask:0xf bound_ctrl:1
	v_cvt_pk_bf16_f32 v50, v162, v163
	v_mov_b32_e32 v109, v1
	v_add_f32_dpp v38, v38, v38 row_shr:2 row_mask:0xf bank_mask:0xf bound_ctrl:1
	v_mov_b32_e32 v166, v1
	v_mul_f32_e32 v167, v119, v119
	v_add_f32_dpp v38, v38, v38 row_shr:4 row_mask:0xf bank_mask:0xf bound_ctrl:1
	v_mul_f32_e32 v168, v122, v122
	v_mul_f32_e32 v169, v123, v123
	v_add_f32_dpp v38, v38, v38 row_shr:8 row_mask:0xf bank_mask:0xf bound_ctrl:1
	s_nop 1
	v_mov_b32_dpp v39, v38 row_bcast:15 row_mask:0xa bank_mask:0xf
	v_add_f32_e32 v38, v38, v39
	v_mov_b32_e32 v39, v1
	s_nop 1
	v_mov_b32_dpp v39, v38 row_bcast:31 row_mask:0xc bank_mask:0xf
	v_add_f32_e32 v38, v38, v39
	s_nop 0
	v_readlane_b32 s0, v38, 63
	s_nop 1
	v_fma_f32 v38, s0, v182, v176
	v_mul_f32_e32 v39, 0x4b800000, v38
	v_cmp_gt_f32_e32 vcc, s51, v38
	s_nop 1
	v_cndmask_b32_e32 v38, v38, v39, vcc
	v_rsq_f32_e32 v38, v38
	s_nop 0
	v_mul_f32_e32 v39, 0x45800000, v38
	v_cndmask_b32_e32 v118, v38, v39, vcc
	v_pk_mul_f32 v[40:41], v[62:63], v[118:119] op_sel_hi:[1,0]
	v_pk_mul_f32 v[38:39], v[64:65], v[118:119] op_sel_hi:[1,0]
	s_waitcnt vmcnt(6)
	v_pk_mul_f32 v[40:41], v[54:55], v[40:41]
	v_mov_b32_e32 v62, v1
	v_pk_fma_f32 v[40:41], v[126:127], v[40:41], v[46:47]
	v_pk_mul_f32 v[38:39], v[56:57], v[38:39]
	v_mul_f32_e32 v51, 0x41800000, v40
	v_mul_f32_e32 v52, 0x41800000, v41
	v_med3_f32 v51, v51, s53, v204
	v_med3_f32 v52, v52, s53, v204
	v_cvt_pk_fp8_f32 v62, v51, v52
	v_pk_fma_f32 v[38:39], v[124:125], v[38:39], v[48:49]
	s_nop 0
	v_mul_f32_e32 v53, 0x41800000, v38
	v_mul_f32_e32 v51, 0x41800000, v39
	v_med3_f32 v52, v53, s53, v204
	v_med3_f32 v51, v51, s53, v204
	v_cvt_pk_fp8_f32 v62, v52, v51 op_sel:[0,0,1]
	v_pk_mul_f32 v[52:53], v[58:59], v[118:119] op_sel_hi:[1,0]
	v_cvt_pk_bf16_f32 v51, v164, v165
	s_waitcnt vmcnt(5)
; DI unsigned pk2(float lo, float hi) { f32x2 v = {lo, hi}; bf16x2v r = __builtin_convertvector(v, bf16x2v); return __builtin_bit_cast(unsigned, r); }
; DI void phase_n1(Frame& F, int l) {
;     ...
;         for (int rr = 0; rr < 2; ++rr) { const int r = blk * 16 + F.wave * 2 + rr;
;             f32x4 (&yv)[4] = yv2[rr]; f32x4 (&xv)[4] = xv2[rr];
;             const float rstd_y = rsqrtf(sumsq(yv, F.lane) * (1.0f / D) + RMS_EPS);
; #pragma unroll
;             for (int j = 0; j < 4; ++j) { const int o = 4 * F.lane + 256 * j; const f32x4 gv = gpm[j], gt = gtm[j];
;                 xv[j] = xv[j] + gt * (yv[j] * rstd_y * gv); u32x2 w; w.x = pk2(xv[j][0], xv[j][1]); w.y = pk2(xv[j][2], xv[j][3]); *(u32x2*)(xb + (size_t)r * D + o) = w; }
;             const float rstd_x = rsqrtf(sumsq(xv, F.lane) * (1.0f / D) + RMS_EPS);
;             mod_norm_store8(xv, rstd_x, mp, h8 + (size_t)r * D, F.lane, hv[rr]); }
	v_pk_mul_f32 v[52:53], v[42:43], v[52:53]
	global_store_dwordx2 v[158:159], v[50:51], off offset:1536 nt
	v_pk_fma_f32 v[52:53], v[116:117], v[52:53], v[34:35]
	v_pk_mul_f32 v[50:51], v[60:61], v[118:119] op_sel_hi:[1,0]
	v_mul_f32_e32 v58, 0x41800000, v52
	v_mul_f32_e32 v59, 0x41800000, v53
	v_pk_mul_f32 v[50:51], v[44:45], v[50:51]
	v_med3_f32 v58, v58, s53, v204
	v_med3_f32 v59, v59, s53, v204
	v_pk_fma_f32 v[50:51], v[114:115], v[50:51], v[36:37]
	v_cvt_pk_fp8_f32 v109, v58, v59
	v_mul_f32_e32 v60, 0x41800000, v50
	v_mul_f32_e32 v58, 0x41800000, v51
	v_med3_f32 v59, v60, s53, v204
	v_pk_mul_f32 v[60:61], v[160:161], v[118:119] op_sel_hi:[1,0]
	v_med3_f32 v58, v58, s53, v204
	s_waitcnt vmcnt(5)
	v_pk_mul_f32 v[60:61], v[30:31], v[60:61]
	v_lshl_add_u64 v[158:159], v[104:105], 0, s[26:27]
	v_cvt_pk_fp8_f32 v109, v59, v58 op_sel:[0,0,1]
	v_pk_mul_f32 v[58:59], v[156:157], v[118:119] op_sel_hi:[1,0]
	v_pk_fma_f32 v[60:61], v[144:145], v[60:61], v[26:27]
	global_store_dword v[158:159], v62, off
	v_pk_mul_f32 v[58:59], v[32:33], v[58:59]
	v_mul_f32_e32 v62, 0x41800000, v60
	v_mul_f32_e32 v63, 0x41800000, v61
	v_pk_fma_f32 v[58:59], v[112:113], v[58:59], v[28:29]
	v_med3_f32 v62, v62, s53, v204
	v_med3_f32 v63, v63, s53, v204
	v_mul_f32_e32 v64, 0x41800000, v58
	v_cvt_pk_fp8_f32 v155, v62, v63
	v_med3_f32 v63, v64, s53, v204
	v_pk_mul_f32 v[64:65], v[162:163], v[118:119] op_sel_hi:[1,0]
	v_mul_f32_e32 v62, 0x41800000, v59
	s_waitcnt vmcnt(5)
	v_pk_mul_f32 v[64:65], v[22:23], v[64:65]
	v_med3_f32 v62, v62, s53, v204
	v_pk_fma_f32 v[64:65], v[142:143], v[64:65], v[18:19]
	v_cvt_pk_fp8_f32 v155, v63, v62 op_sel:[0,0,1]
	v_pk_mul_f32 v[62:63], v[164:165], v[118:119] op_sel_hi:[1,0]
	v_mul_f32_e32 v118, 0x41800000, v64
	v_mul_f32_e32 v120, 0x41800000, v65
	v_med3_f32 v118, v118, s53, v204
	v_med3_f32 v120, v120, s53, v204
	v_pk_mul_f32 v[62:63], v[24:25], v[62:63]
	v_cvt_pk_fp8_f32 v166, v118, v120
	v_pk_fma_f32 v[62:63], v[140:141], v[62:63], v[20:21]
	v_pk_mul_f32 v[160:161], v[134:135], v[134:135]
	v_mul_f32_e32 v156, 0x41800000, v62
	v_mul_f32_e32 v118, 0x41800000, v63
	v_med3_f32 v120, v156, s53, v204
	v_med3_f32 v118, v118, s53, v204
	v_cvt_pk_fp8_f32 v166, v120, v118 op_sel:[0,0,1]
	v_mul_f32_e32 v118, v139, v139
	v_pk_fma_f32 v[156:157], v[138:139], v[138:139], v[118:119] op_sel_hi:[1,1,0]
	v_mul_f32_e32 v118, v137, v137
	v_pk_fma_f32 v[162:163], v[136:137], v[136:137], v[118:119] op_sel_hi:[1,1,0]
	v_pk_fma_f32 v[160:161], v[132:133], v[132:133], v[160:161]
	v_mov_b32_e32 v120, v162
	v_mov_b32_e32 v164, v156
	v_mov_b32_e32 v165, v121
	v_pk_add_f32 v[156:157], v[162:163], v[156:157]
	v_pk_mul_f32 v[162:163], v[120:121], v[164:165]
	v_pk_add_f32 v[160:161], v[160:161], v[160:161] op_sel:[0,1] op_sel_hi:[1,0]
	v_mov_b32_e32 v157, v163
	v_mov_b32_e32 v161, v167
	v_mul_f32_e32 v118, v129, v129
	v_pk_add_f32 v[156:157], v[156:157], v[160:161]
	v_pk_fma_f32 v[160:161], v[128:129], v[128:129], v[118:119] op_sel_hi:[1,1,0]
	v_mul_f32_e32 v118, v131, v131
	v_pk_fma_f32 v[162:163], v[130:131], v[130:131], v[118:119] op_sel_hi:[1,1,0]
	v_mov_b32_e32 v161, v168
	v_mov_b32_e32 v163, v169
	v_pk_add_f32 v[160:161], v[160:161], v[162:163]
	v_mov_b32_e32 v120, v1
	v_pk_add_f32 v[156:157], v[156:157], v[160:161]
	global_store_dword v[158:159], v109, off offset:256
	global_store_dword v[158:159], v155, off offset:512
	global_store_dword v[158:159], v166, off offset:768
	v_add_f32_e32 v118, v156, v157
	s_nop 1
	v_add_f32_dpp v118, v118, v118 row_shr:1 row_mask:0xf bank_mask:0xf bound_ctrl:1
	s_nop 1
	v_add_f32_dpp v118, v118, v118 row_shr:2 row_mask:0xf bank_mask:0xf bound_ctrl:1
	s_nop 1
	v_add_f32_dpp v118, v118, v118 row_shr:4 row_mask:0xf bank_mask:0xf bound_ctrl:1
	s_nop 1
	v_add_f32_dpp v118, v118, v118 row_shr:8 row_mask:0xf bank_mask:0xf bound_ctrl:1
	s_nop 1
	v_mov_b32_dpp v120, v118 row_bcast:15 row_mask:0xa bank_mask:0xf
	v_add_f32_e32 v118, v118, v120
	v_mov_b32_e32 v120, v1
	s_nop 1
	v_mov_b32_dpp v120, v118 row_bcast:31 row_mask:0xc bank_mask:0xf
	v_add_f32_e32 v118, v118, v120
	s_nop 0
	v_readlane_b32 s0, v118, 63
	s_nop 1
	v_fma_f32 v118, s0, v182, v176
	v_mul_f32_e32 v120, 0x4b800000, v118
	v_cmp_gt_f32_e32 vcc, s51, v118
	s_nop 1
	v_cndmask_b32_e32 v118, v118, v120, vcc
	v_rsq_f32_e32 v118, v118
	s_nop 0
	v_mul_f32_e32 v109, 0x45800000, v118
	v_cndmask_b32_e32 v120, v118, v109, vcc
	v_pk_mul_f32 v[138:139], v[120:121], v[138:139] op_sel_hi:[0,1]
	v_pk_mul_f32 v[136:137], v[120:121], v[136:137] op_sel_hi:[0,1]
	v_pk_mul_f32 v[70:71], v[70:71], v[136:137]
	v_pk_mul_f32 v[72:73], v[72:73], v[138:139]
	v_pk_fma_f32 v[14:15], v[74:75], v[70:71], v[14:15]
	v_pk_fma_f32 v[16:17], v[76:77], v[72:73], v[16:17]
	v_cvt_pk_bf16_f32 v70, v14, v15
	v_cvt_pk_bf16_f32 v71, v16, v17
	v_lshl_add_u64 v[72:73], v[100:101], 0, s[14:15]
	global_store_dwordx2 v[72:73], v[70:71], off nt
	v_mov_b32_e32 v70, v133
	v_mov_b32_e32 v71, v135
	v_mov_b32_e32 v133, v134
	v_pk_mul_f32 v[70:71], v[120:121], v[70:71] op_sel_hi:[0,1]
	v_pk_mul_f32 v[74:75], v[120:121], v[132:133] op_sel_hi:[0,1]
	v_pk_mul_f32 v[74:75], v[94:95], v[74:75]
	v_pk_mul_f32 v[70:71], v[96:97], v[70:71]
	v_pk_fma_f32 v[10:11], v[90:91], v[74:75], v[10:11]
	v_pk_fma_f32 v[12:13], v[92:93], v[70:71], v[12:13]
	v_cvt_pk_bf16_f32 v70, v10, v11
	v_cvt_pk_bf16_f32 v71, v12, v13
	global_store_dwordx2 v[72:73], v[70:71], off offset:512 nt
	v_pk_mul_f32 v[70:71], v[120:121], v[130:131] op_sel_hi:[0,1]
	v_pk_mul_f32 v[74:75], v[120:121], v[128:129] op_sel_hi:[0,1]
	v_pk_mul_f32 v[74:75], v[86:87], v[74:75]
	v_pk_mul_f32 v[70:71], v[88:89], v[70:71]
	v_pk_fma_f32 v[6:7], v[82:83], v[74:75], v[6:7]
; #define LAS __attribute__((address_space(3)))
; DI unsigned pk2(float lo, float hi) { f32x2 v = {lo, hi}; bf16x2v r = __builtin_convertvector(v, bf16x2v); return __builtin_bit_cast(unsigned, r); }
; DI void phase_n1(Frame& F, int l) {
;     ...
;             for (int j = 0; j < 4; ++j) { const int o = 4 * F.lane + 256 * j; const f32x4 gv = gpm[j], gt = gtm[j];
;                 xv[j] = xv[j] + gt * (yv[j] * rstd_y * gv); u32x2 w; w.x = pk2(xv[j][0], xv[j][1]); w.y = pk2(xv[j][2], xv[j][3]); *(u32x2*)(xb + (size_t)r * D + o) = w; }
;             const float rstd_x = rsqrtf(sumsq(xv, F.lane) * (1.0f / D) + RMS_EPS);
;             mod_norm_store8(xv, rstd_x, mp, h8 + (size_t)r * D, F.lane, hv[rr]); }
; #pragma unroll
;         for (int rr = 0; rr < 2; ++rr)
; #pragma unroll
;             for (int j = 0; j < 4; ++j) { u32x2 w; w.x = pk2(hv[rr][j][0], hv[rr][j][1]); w.y = pk2(hv[rr][j][2], hv[rr][j][3]); *(LAS u32x2*)(HTl + (F.wave * 2 + rr) * RP + (4 * F.lane + 256 * j) * 2) = w; }
;         __syncthreads();
	v_pk_fma_f32 v[8:9], v[84:85], v[70:71], v[8:9]
	v_cvt_pk_bf16_f32 v70, v6, v7
	v_cvt_pk_bf16_f32 v71, v8, v9
	v_mov_b32_e32 v118, v121
	global_store_dwordx2 v[72:73], v[70:71], off offset:1024 nt
	v_pk_mul_f32 v[70:71], v[120:121], v[122:123] op_sel_hi:[0,1]
	v_pk_mul_f32 v[74:75], v[120:121], v[118:119] op_sel_hi:[0,1]
	v_pk_mul_f32 v[74:75], v[78:79], v[74:75]
	v_pk_mul_f32 v[70:71], v[80:81], v[70:71]
	v_pk_fma_f32 v[2:3], v[66:67], v[74:75], v[2:3]
	v_pk_fma_f32 v[4:5], v[68:69], v[70:71], v[4:5]
	v_pk_mul_f32 v[66:67], v[16:17], v[16:17]
	v_pk_mul_f32 v[68:69], v[14:15], v[14:15]
	s_nop 0
	v_pk_mov_b32 v[70:71], v[68:69], v[66:67] op_sel:[1,0]
	v_mov_b32_e32 v69, v67
	v_pk_add_f32 v[66:67], v[70:71], v[68:69]
	v_pk_mul_f32 v[68:69], v[12:13], v[12:13]
	v_pk_add_f32 v[66:67], v[66:67], v[66:67] op_sel_hi:[0,1]
	v_pk_mul_f32 v[70:71], v[10:11], v[10:11]
	v_mul_f32_e32 v66, v6, v6
	v_pk_mov_b32 v[74:75], v[70:71], v[68:69] op_sel:[1,0]
	v_mov_b32_e32 v71, v69
	v_pk_add_f32 v[68:69], v[74:75], v[70:71]
	v_pk_fma_f32 v[70:71], v[6:7], v[6:7], v[66:67] op_sel_hi:[1,1,0]
	v_mul_f32_e32 v66, v8, v8
	v_pk_add_f32 v[68:69], v[68:69], v[68:69] op_sel_hi:[0,1]
	v_pk_fma_f32 v[74:75], v[8:9], v[8:9], v[66:67] op_sel_hi:[1,1,0]
	v_mul_f32_e32 v70, v2, v2
	v_mul_f32_e32 v74, v3, v3
	v_mul_f32_e32 v66, v4, v4
	v_mul_f32_e32 v68, v5, v5
	v_pk_add_f32 v[70:71], v[70:71], v[74:75]
	v_pk_add_f32 v[66:67], v[66:67], v[68:69]
	s_nop 0
	v_pk_add_f32 v[66:67], v[70:71], v[66:67]
	s_nop 0
	v_add_f32_e32 v66, v66, v67
	v_mov_b32_e32 v67, v1
	s_nop 0
	v_add_f32_dpp v66, v66, v66 row_shr:1 row_mask:0xf bank_mask:0xf bound_ctrl:1
	s_nop 1
	v_add_f32_dpp v66, v66, v66 row_shr:2 row_mask:0xf bank_mask:0xf bound_ctrl:1
	s_nop 1
	v_add_f32_dpp v66, v66, v66 row_shr:4 row_mask:0xf bank_mask:0xf bound_ctrl:1
	s_nop 1
	v_add_f32_dpp v66, v66, v66 row_shr:8 row_mask:0xf bank_mask:0xf bound_ctrl:1
	s_nop 1
	v_mov_b32_dpp v67, v66 row_bcast:15 row_mask:0xa bank_mask:0xf
	v_add_f32_e32 v66, v66, v67
	v_mov_b32_e32 v67, v1
	s_nop 1
	v_mov_b32_dpp v67, v66 row_bcast:31 row_mask:0xc bank_mask:0xf
	v_add_f32_e32 v66, v66, v67
	s_nop 0
	v_readlane_b32 s0, v66, 63
	s_nop 1
	v_fma_f32 v66, s0, v182, v176
	v_mul_f32_e32 v67, 0x4b800000, v66
	v_cmp_gt_f32_e32 vcc, s51, v66
	s_nop 1
	v_cndmask_b32_e32 v66, v66, v67, vcc
	v_rsq_f32_e32 v68, v66
	v_cvt_pk_bf16_f32 v66, v2, v3
	v_cvt_pk_bf16_f32 v67, v4, v5
	global_store_dwordx2 v[72:73], v[66:67], off offset:1536 nt
	v_mul_f32_e32 v66, 0x45800000, v68
	v_cndmask_b32_e32 v66, v68, v66, vcc
	v_pk_mul_f32 v[14:15], v[14:15], v[66:67] op_sel_hi:[1,0]
	v_pk_mul_f32 v[10:11], v[10:11], v[66:67] op_sel_hi:[1,0]
	v_pk_mul_f32 v[14:15], v[54:55], v[14:15]
	v_pk_mul_f32 v[16:17], v[16:17], v[66:67] op_sel_hi:[1,0]
	v_pk_fma_f32 v[14:15], v[126:127], v[14:15], v[46:47]
	v_pk_mul_f32 v[10:11], v[42:43], v[10:11]
	v_pk_mul_f32 v[6:7], v[6:7], v[66:67] op_sel_hi:[1,0]
	v_pk_mul_f32 v[16:17], v[56:57], v[16:17]
	v_mul_f32_e32 v46, 0x41800000, v14
	v_mul_f32_e32 v47, 0x41800000, v15
	v_pk_mul_f32 v[12:13], v[12:13], v[66:67] op_sel_hi:[1,0]
	v_pk_fma_f32 v[10:11], v[116:117], v[10:11], v[34:35]
	v_pk_mul_f32 v[6:7], v[30:31], v[6:7]
	v_pk_mul_f32 v[2:3], v[2:3], v[66:67] op_sel_hi:[1,0]
	v_pk_fma_f32 v[16:17], v[124:125], v[16:17], v[48:49]
	v_med3_f32 v46, v46, s53, v204
	v_med3_f32 v47, v47, s53, v204
	v_mov_b32_e32 v49, v1
	v_pk_mul_f32 v[12:13], v[44:45], v[12:13]
	v_mul_f32_e32 v34, 0x41800000, v10
	v_mul_f32_e32 v35, 0x41800000, v11
	v_pk_mul_f32 v[8:9], v[8:9], v[66:67] op_sel_hi:[1,0]
	v_pk_fma_f32 v[6:7], v[144:145], v[6:7], v[26:27]
	v_pk_mul_f32 v[2:3], v[22:23], v[2:3]
	v_cvt_pk_fp8_f32 v49, v46, v47
	v_pk_fma_f32 v[12:13], v[114:115], v[12:13], v[36:37]
	v_med3_f32 v34, v34, s53, v204
	v_med3_f32 v35, v35, s53, v204
	v_mov_b32_e32 v37, v1
	v_pk_mul_f32 v[8:9], v[32:33], v[8:9]
	v_mul_f32_e32 v26, 0x41800000, v6
	v_mul_f32_e32 v27, 0x41800000, v7
	v_pk_mul_f32 v[4:5], v[4:5], v[66:67] op_sel_hi:[1,0]
	v_pk_fma_f32 v[2:3], v[142:143], v[2:3], v[18:19]
	v_cvt_pk_fp8_f32 v37, v34, v35
	v_pk_fma_f32 v[8:9], v[112:113], v[8:9], v[28:29]
	v_med3_f32 v26, v26, s53, v204
	v_med3_f32 v27, v27, s53, v204
	v_mov_b32_e32 v29, v1
	v_pk_mul_f32 v[4:5], v[24:25], v[4:5]
	v_mul_f32_e32 v18, 0x41800000, v2
	v_mul_f32_e32 v19, 0x41800000, v3
	v_mul_f32_e32 v48, 0x41800000, v16
	v_mul_f32_e32 v46, 0x41800000, v17
	v_cvt_pk_fp8_f32 v29, v26, v27
	v_pk_fma_f32 v[4:5], v[140:141], v[4:5], v[20:21]
	v_med3_f32 v18, v18, s53, v204
	v_med3_f32 v19, v19, s53, v204
	v_mov_b32_e32 v21, v1
	v_med3_f32 v47, v48, s53, v204
	v_med3_f32 v46, v46, s53, v204
	v_mul_f32_e32 v36, 0x41800000, v12
	v_mul_f32_e32 v34, 0x41800000, v13
	v_cvt_pk_fp8_f32 v21, v18, v19
	v_cvt_pk_fp8_f32 v49, v47, v46 op_sel:[0,0,1]
	v_med3_f32 v35, v36, s53, v204
	v_med3_f32 v34, v34, s53, v204
	v_mul_f32_e32 v28, 0x41800000, v8
	v_mul_f32_e32 v26, 0x41800000, v9
	v_cvt_pk_fp8_f32 v37, v35, v34 op_sel:[0,0,1]
	v_med3_f32 v27, v28, s53, v204
	v_med3_f32 v26, v26, s53, v204
	v_mul_f32_e32 v20, 0x41800000, v4
	v_mul_f32_e32 v18, 0x41800000, v5
	v_cvt_pk_fp8_f32 v29, v27, v26 op_sel:[0,0,1]
	v_med3_f32 v19, v20, s53, v204
	v_med3_f32 v18, v18, s53, v204
	v_lshl_add_u64 v[46:47], v[104:105], 0, s[2:3]
	v_cvt_pk_fp8_f32 v21, v19, v18 op_sel:[0,0,1]
	global_store_dword v[46:47], v49, off
	global_store_dword v[46:47], v37, off offset:256
	global_store_dword v[46:47], v29, off offset:512
	global_store_dword v[46:47], v21, off offset:768
	v_cvt_pk_bf16_f32 v18, v40, v41
	v_cvt_pk_bf16_f32 v19, v38, v39
	v_cvt_pk_bf16_f32 v20, v52, v53
	v_cvt_pk_bf16_f32 v21, v50, v51
	ds_write2st64_b64 v150, v[18:19], v[20:21] offset1:1
	v_cvt_pk_bf16_f32 v18, v60, v61
	v_cvt_pk_bf16_f32 v19, v58, v59
	v_cvt_pk_bf16_f32 v20, v64, v65
	v_cvt_pk_bf16_f32 v21, v62, v63
	v_cvt_pk_bf16_f32 v14, v14, v15
	v_cvt_pk_bf16_f32 v15, v16, v17
	v_cvt_pk_bf16_f32 v10, v10, v11
	v_cvt_pk_bf16_f32 v11, v12, v13
	v_add_u32_e32 v12, 16, v150
	v_cvt_pk_bf16_f32 v6, v6, v7
	v_cvt_pk_bf16_f32 v7, v8, v9
	v_cvt_pk_bf16_f32 v2, v2, v3
	v_cvt_pk_bf16_f32 v3, v4, v5
	ds_write2st64_b64 v150, v[18:19], v[20:21] offset0:2 offset1:3
	ds_write2st64_b64 v12, v[14:15], v[10:11] offset0:4 offset1:5
	ds_write2st64_b64 v12, v[6:7], v[2:3] offset0:6 offset1:7
	s_waitcnt lgkmcnt(0)
	s_barrier
; #define LAS __attribute__((address_space(3)))
; DI void phase_n1(Frame& F, int l) {
;     ...
;         { const int r16 = F.lane & 15, kg = F.lane >> 4; f32x4 c0 = (f32x4){0.f, 0.f, 0.f, 0.f}, c1 = c0;
; #pragma unroll
;           for (int st = 0; st < 4; ++st) { const int kb2 = (128 * F.wave + 32 * st + 8 * kg) * 2;
;               const bf16x8 af = *(const LAS bf16x8*)(HTl + r16 * RP + kb2), b0 = *(const LAS bf16x8*)(WTl + r16 * RP + kb2), b1 = *(const LAS bf16x8*)(WTl + (16 + r16) * RP + kb2);
;               c0 = __builtin_amdgcn_mfma_f32_16x16x32_bf16(af, b0, c0, 0, 0, 0); c1 = __builtin_amdgcn_mfma_f32_16x16x32_bf16(af, b1, c1, 0, 0, 0); }
; #pragma unroll
;           for (int i = 0; i < 4; ++i) { PS[(F.wave * 16 + 4 * kg + i) * 32 + r16] = c0[i]; PS[(F.wave * 16 + 4 * kg + i) * 32 + 16 + r16] = c1[i]; } }
;         __syncthreads();
;         float lgs = 0.f;
; #pragma unroll
;         for (int w = 0; w < 8; ++w) lgs += PS[(w * 16 + F.wave * 2 + (F.lane >> 5)) * 32 + (F.lane & 31)];
;         float lg = lgs + brt; const int e_me = F.lane & 31;
;         float topv[4]; int tope[4];
; #pragma unroll
;         for (int k = 0; k < 4; ++k) { float mv = lg; int mi = e_me;
; #pragma unroll
;             for (int st = 0; st < 4; ++st) {
;                 float ov; int oi;
;                 if (st == 0) { ov = __int_as_float(__builtin_amdgcn_update_dpp(0, __float_as_int(mv), 0x121, 0xf, 0xf, false)); oi = __builtin_amdgcn_update_dpp(0, mi, 0x121, 0xf, 0xf, false); }
;                 else if (st == 1) { ov = __int_as_float(__builtin_amdgcn_update_dpp(0, __float_as_int(mv), 0x122, 0xf, 0xf, false)); oi = __builtin_amdgcn_update_dpp(0, mi, 0x122, 0xf, 0xf, false); }
;                 else if (st == 2) { ov = __int_as_float(__builtin_amdgcn_update_dpp(0, __float_as_int(mv), 0x124, 0xf, 0xf, false)); oi = __builtin_amdgcn_update_dpp(0, mi, 0x124, 0xf, 0xf, false); }
;                 else { ov = __int_as_float(__builtin_amdgcn_update_dpp(0, __float_as_int(mv), 0x128, 0xf, 0xf, false)); oi = __builtin_amdgcn_update_dpp(0, mi, 0x128, 0xf, 0xf, false); }
;                 if (ov > mv || (ov == mv && oi < mi)) { mv = ov; mi = oi; } }
;             { const float ov = shx(mv, 16, F.lane); const int oi = shxi(mi, 16, F.lane); if (ov > mv || (ov == mv && oi < mi)) { mv = ov; mi = oi; } }
	ds_read_b128 v[2:5], v151
	ds_read_b128 v[6:9], v152
	ds_read_b128 v[10:13], v151 offset:64
	ds_read_b128 v[14:17], v152 offset:64
	s_waitcnt lgkmcnt(2)
	v_mfma_f32_16x16x32_bf16 v[6:9], v[2:5], v[6:9], 0
	ds_read_b128 v[18:21], v152 offset:33024
	ds_read_b128 v[22:25], v152 offset:33088
	s_waitcnt lgkmcnt(2)
	v_mfma_f32_16x16x32_bf16 v[6:9], v[10:13], v[14:17], v[6:9]
	ds_read_b128 v[14:17], v151 offset:128
	s_waitcnt lgkmcnt(2)
	v_mfma_f32_16x16x32_bf16 v[2:5], v[2:5], v[18:21], 0
	s_waitcnt lgkmcnt(1)
	v_mfma_f32_16x16x32_bf16 v[2:5], v[10:13], v[22:25], v[2:5]
	ds_read_b128 v[10:13], v152 offset:128
	ds_read_b128 v[18:21], v151 offset:192
	ds_read_b128 v[22:25], v152 offset:192
	s_waitcnt lgkmcnt(2)
	v_mfma_f32_16x16x32_bf16 v[6:9], v[14:17], v[10:13], v[6:9]
	ds_read_b128 v[10:13], v152 offset:33152
	ds_read_b128 v[26:29], v152 offset:33216
	s_waitcnt lgkmcnt(1)
	v_mfma_f32_16x16x32_bf16 v[2:5], v[14:17], v[10:13], v[2:5]
	v_mfma_f32_16x16x32_bf16 v[6:9], v[18:21], v[22:25], v[6:9]
	s_waitcnt lgkmcnt(0)
	v_mfma_f32_16x16x32_bf16 v[2:5], v[18:21], v[26:29], v[2:5]
	s_nop 7
	ds_write2_b32 v153, v6, v2 offset1:16
	ds_write2_b32 v153, v7, v3 offset0:32 offset1:48
	ds_write2_b32 v153, v8, v4 offset0:64 offset1:80
	ds_write2_b32 v153, v9, v5 offset0:96 offset1:112
	s_waitcnt lgkmcnt(0)
	s_barrier
	ds_read2st64_b32 v[2:3], v154 offset1:8
	ds_read2st64_b32 v[4:5], v154 offset0:16 offset1:24
	ds_read2st64_b32 v[6:7], v154 offset0:32 offset1:40
	s_waitcnt lgkmcnt(2)
	v_add_f32_e32 v2, 0, v2
	v_add_f32_e32 v8, v2, v3
	ds_read2st64_b32 v[2:3], v154 offset0:48 offset1:56
	s_waitcnt lgkmcnt(2)
	v_add_f32_e32 v4, v8, v4
	v_add_f32_e32 v4, v4, v5
	s_waitcnt lgkmcnt(1)
	v_add_f32_e32 v4, v4, v6
	v_add_f32_e32 v4, v4, v7
	s_waitcnt lgkmcnt(0)
	v_add_f32_e32 v2, v4, v2
	v_add_f32_e32 v2, v2, v3
	v_add_f32_e32 v4, v0, v2
	v_mov_b32_e32 v6, v1
	v_mov_b32_e32 v7, v1
	s_nop 0
	v_mov_b32_dpp v6, v4 row_ror:1 row_mask:0xf bank_mask:0xf
	v_mov_b32_dpp v7, v146 row_ror:1 row_mask:0xf bank_mask:0xf
	v_cmp_lt_f32_e64 s[2:3], v4, v6
	v_cmp_nlt_f32_e32 vcc, v4, v6
	s_and_saveexec_b64 s[16:17], vcc
	v_cmp_eq_f32_e32 vcc, v4, v6
	v_cmp_lt_i32_e64 s[14:15], v7, v146
	s_and_b64 s[0:1], vcc, s[14:15]
	s_andn2_b64 s[2:3], s[2:3], exec
	s_and_b64 s[0:1], s[0:1], exec
	s_or_b64 s[2:3], s[2:3], s[0:1]
	s_or_b64 exec, exec, s[16:17]
	v_mov_b32_e32 v5, v4
	v_mov_b32_e32 v3, v4
	v_mov_b32_e32 v2, v146
	s_and_saveexec_b64 s[14:15], s[2:3]
	v_mov_b32_e32 v5, v6
	v_mov_b32_e32 v3, v6
	v_mov_b32_e32 v2, v7
	s_or_b64 exec, exec, s[14:15]
	v_mov_b32_e32 v6, v1
	v_mov_b32_e32 v7, v1
	s_nop 0
	v_mov_b32_dpp v6, v5 row_ror:2 row_mask:0xf bank_mask:0xf
	v_mov_b32_dpp v7, v2 row_ror:2 row_mask:0xf bank_mask:0xf
	v_cmp_lt_f32_e64 s[2:3], v3, v6
	v_cmp_nlt_f32_e32 vcc, v3, v6
	s_and_saveexec_b64 s[16:17], vcc
	v_cmp_eq_f32_e32 vcc, v3, v6
	v_cmp_lt_i32_e64 s[14:15], v7, v2
	s_and_b64 s[0:1], vcc, s[14:15]
	s_andn2_b64 s[2:3], s[2:3], exec
	s_and_b64 s[0:1], s[0:1], exec
	s_or_b64 s[2:3], s[2:3], s[0:1]
	s_or_b64 exec, exec, s[16:17]
	s_and_saveexec_b64 s[14:15], s[2:3]
	v_mov_b32_e32 v5, v6
	v_mov_b32_e32 v3, v6
	v_mov_b32_e32 v2, v7
	s_or_b64 exec, exec, s[14:15]
	v_mov_b32_e32 v6, v1
	v_mov_b32_e32 v7, v1
	s_nop 0
	v_mov_b32_dpp v6, v5 row_ror:4 row_mask:0xf bank_mask:0xf
	v_mov_b32_dpp v7, v2 row_ror:4 row_mask:0xf bank_mask:0xf
	v_cmp_lt_f32_e64 s[2:3], v3, v6
	v_cmp_nlt_f32_e32 vcc, v3, v6
	s_and_saveexec_b64 s[16:17], vcc
	v_cmp_eq_f32_e32 vcc, v3, v6
	v_cmp_lt_i32_e64 s[14:15], v7, v2
	s_and_b64 s[0:1], vcc, s[14:15]
	s_andn2_b64 s[2:3], s[2:3], exec
	s_and_b64 s[0:1], s[0:1], exec
	s_or_b64 s[2:3], s[2:3], s[0:1]
	s_or_b64 exec, exec, s[16:17]
	s_and_saveexec_b64 s[14:15], s[2:3]
	v_mov_b32_e32 v5, v6
	v_mov_b32_e32 v3, v6
	v_mov_b32_e32 v2, v7
	s_or_b64 exec, exec, s[14:15]
	v_mov_b32_e32 v6, v1
	v_mov_b32_e32 v7, v1
	s_nop 0
	v_mov_b32_dpp v6, v5 row_ror:8 row_mask:0xf bank_mask:0xf
	v_mov_b32_dpp v7, v2 row_ror:8 row_mask:0xf bank_mask:0xf
	v_cmp_lt_f32_e64 s[2:3], v3, v6
	v_cmp_nlt_f32_e32 vcc, v3, v6
	s_and_saveexec_b64 s[16:17], vcc
	v_cmp_eq_f32_e32 vcc, v3, v6
	v_cmp_lt_i32_e64 s[14:15], v7, v2
	s_and_b64 s[0:1], vcc, s[14:15]
	s_andn2_b64 s[2:3], s[2:3], exec
	s_and_b64 s[0:1], s[0:1], exec
	s_or_b64 s[2:3], s[2:3], s[0:1]
	s_or_b64 exec, exec, s[16:17]
	s_and_saveexec_b64 s[14:15], s[2:3]
	v_mov_b32_e32 v5, v6
	v_mov_b32_e32 v3, v6
	v_mov_b32_e32 v2, v7
	s_or_b64 exec, exec, s[14:15]
	ds_bpermute_b32 v5, v148, v5
	ds_bpermute_b32 v6, v148, v2
	s_waitcnt lgkmcnt(1)
	v_cmp_lt_f32_e64 s[2:3], v3, v5
	v_cmp_nlt_f32_e32 vcc, v3, v5
	s_and_saveexec_b64 s[16:17], vcc
	s_cbranch_execz .LBB0_1058
	v_cmp_eq_f32_e32 vcc, v3, v5
	s_waitcnt lgkmcnt(0)
	v_cmp_lt_i32_e64 s[14:15], v6, v2
	s_and_b64 s[0:1], vcc, s[14:15]
	s_andn2_b64 s[2:3], s[2:3], exec
	s_and_b64 s[0:1], s[0:1], exec
	s_or_b64 s[2:3], s[2:3], s[0:1]

; DI unsigned pk2(float lo, float hi) { f32x2 v = {lo, hi}; bf16x2v r = __builtin_convertvector(v, bf16x2v); return __builtin_bit_cast(unsigned, r); }
; #define DPP_ADD_(ctrl, rmask, bc) v += __int_as_float(__builtin_amdgcn_update_dpp(0, __float_as_int(v), ctrl, rmask, 0xf, bc))
; DI float wave_sum_dpp(float v) {
;     ...
;     DPP_ADD_(0x111, 0xf, true); DPP_ADD_(0x112, 0xf, true); DPP_ADD_(0x114, 0xf, true); DPP_ADD_(0x118, 0xf, true);
;     DPP_ADD_(0x142, 0xa, false); DPP_ADD_(0x143, 0xc, false);
;     ...
;     return __int_as_float(__builtin_amdgcn_readlane(__float_as_int(v), 63)); }
; #pragma unroll
;     for (int j = 0; j < 4; ++j) s += (v[j][0] * v[j][0] + v[j][1] * v[j][1]) + (v[j][2] * v[j][2] + v[j][3] * v[j][3]);
;     return wave_sum_dpp(s); }
; DI void phase_n2(Frame& F, int l) {
;     ...
;         for (int rr = 0; rr < 2; ++rr) { const int r = r0 + rr;
;             f32x4 yv[4], hv[4]; f32x4 (&xv)[4] = xa[rr];
; #pragma unroll
;             for (int j = 0; j < 4; ++j) yv[j] = ((ya[rr][0][j] + ya[rr][1][j]) + (ya[rr][2][j] + ya[rr][3][j])) * (1.0f / YS8_SCALE);
;             const float rstd_y = rsqrtf(sumsq(yv, F.lane) * (1.0f / D) + RMS_EPS);
; #pragma unroll
;             for (int j = 0; j < 4; ++j) { const int o = 4 * F.lane + 256 * j; const f32x4 gv = gpf[j], gt = gtf[j];
;                 xv[j] = xv[j] + gt * (yv[j] * rstd_y * gv);
;                 if (l + 1 < DEPTH) { u32x2 w; w.x = pk2(xv[j][0], xv[j][1]); w.y = pk2(xv[j][2], xv[j][3]); *(u32x2*)(xb + (size_t)r * D + o) = w; } else *(f32x4*)(F.out + (size_t)r * D + o) = xv[j]; }
.LBB0_1402:
	s_waitcnt vmcnt(0)
	v_cvt_pk_f32_fp8_e32 v[130:131], v129
	v_cvt_pk_f32_fp8_e32 v[162:163], v92
	v_cvt_pk_f32_fp8_e32 v[164:165], v89
	v_cvt_pk_f32_fp8_sdwa v[166:167], v89 src0_sel:WORD_1
	v_cvt_pk_f32_fp8_e32 v[168:169], v88
	v_cvt_pk_f32_fp8_sdwa v[170:171], v88 src0_sel:WORD_1
	v_cvt_pk_f32_fp8_e32 v[88:89], v84
	v_cvt_pk_f32_fp8_e32 v[184:185], v125
	v_cvt_pk_f32_fp8_sdwa v[132:133], v129 src0_sel:WORD_1
	v_cvt_pk_f32_fp8_e32 v[158:159], v93
	v_cvt_pk_f32_fp8_sdwa v[160:161], v93 src0_sel:WORD_1
	v_cvt_pk_f32_fp8_sdwa v[92:93], v92 src0_sel:WORD_1
	v_cvt_pk_f32_fp8_e32 v[172:173], v85
	v_cvt_pk_f32_fp8_sdwa v[174:175], v85 src0_sel:WORD_1
	v_cvt_pk_f32_fp8_sdwa v[84:85], v84 src0_sel:WORD_1
	v_cvt_pk_f32_fp8_sdwa v[186:187], v125 src0_sel:WORD_1
	v_cvt_pk_f32_fp8_e32 v[134:135], v123
	v_cvt_pk_f32_fp8_sdwa v[136:137], v123 src0_sel:WORD_1
	v_cvt_pk_f32_fp8_e32 v[176:177], v128
	v_cvt_pk_f32_fp8_sdwa v[128:129], v128 src0_sel:WORD_1
	v_cvt_pk_f32_fp8_e32 v[188:189], v124
	v_cvt_pk_f32_fp8_sdwa v[124:125], v124 src0_sel:WORD_1
	v_cvt_pk_f32_fp8_e32 v[154:155], v97
	v_cvt_pk_f32_fp8_e32 v[178:179], v127
	v_cvt_pk_f32_fp8_e32 v[190:191], v122
	v_cvt_pk_f32_fp8_sdwa v[156:157], v97 src0_sel:WORD_1
	v_cvt_pk_f32_fp8_sdwa v[180:181], v127 src0_sel:WORD_1
	v_cvt_pk_f32_fp8_sdwa v[122:123], v122 src0_sel:WORD_1
	v_pk_add_f32 v[130:131], v[130:131], v[162:163]
	v_pk_add_f32 v[88:89], v[88:89], v[184:185]
	v_cvt_pk_f32_fp8_e32 v[182:183], v126
	v_cvt_pk_f32_fp8_sdwa v[126:127], v126 src0_sel:WORD_1
	v_cvt_pk_f32_fp8_e32 v[192:193], v96
	v_cvt_pk_f32_fp8_sdwa v[96:97], v96 src0_sel:WORD_1
	v_pk_add_f32 v[92:93], v[132:133], v[92:93]
	v_pk_add_f32 v[84:85], v[84:85], v[186:187]
	v_pk_add_f32 v[88:89], v[130:131], v[88:89]
	v_pk_add_f32 v[84:85], v[92:93], v[84:85]
	v_pk_mul_f32 v[130:131], v[88:89], s[16:17] op_sel_hi:[1,0]
	v_pk_add_f32 v[88:89], v[134:135], v[164:165]
	v_pk_add_f32 v[92:93], v[136:137], v[166:167]
	v_pk_add_f32 v[132:133], v[176:177], v[188:189]
	v_pk_add_f32 v[124:125], v[128:129], v[124:125]
	v_pk_add_f32 v[128:129], v[88:89], v[132:133]
	v_pk_add_f32 v[88:89], v[92:93], v[124:125]
	v_pk_add_f32 v[92:93], v[154:155], v[168:169]
	v_pk_add_f32 v[132:133], v[178:179], v[190:191]
	v_pk_add_f32 v[124:125], v[156:157], v[170:171]
	v_pk_add_f32 v[122:123], v[180:181], v[122:123]
	v_pk_add_f32 v[132:133], v[92:93], v[132:133]
	v_pk_mul_f32 v[84:85], v[84:85], s[16:17] op_sel_hi:[1,0]
	v_pk_add_f32 v[92:93], v[124:125], v[122:123]
	v_pk_mul_f32 v[124:125], v[132:133], s[16:17] op_sel_hi:[1,0]
	v_pk_add_f32 v[132:133], v[160:161], v[174:175]
	v_pk_add_f32 v[96:97], v[126:127], v[96:97]
	v_pk_add_f32 v[122:123], v[158:159], v[172:173]
	v_pk_add_f32 v[134:135], v[182:183], v[192:193]
	v_pk_add_f32 v[96:97], v[132:133], v[96:97]
	v_pk_mul_f32 v[126:127], v[84:85], v[84:85]
	v_pk_mul_f32 v[132:133], v[130:131], v[130:131]
	v_pk_mul_f32 v[88:89], v[88:89], s[16:17] op_sel_hi:[1,0]
	v_pk_mul_f32 v[128:129], v[128:129], s[16:17] op_sel_hi:[1,0]
	v_pk_add_f32 v[122:123], v[122:123], v[134:135]
	v_pk_mov_b32 v[134:135], v[132:133], v[126:127] op_sel:[1,0]
	v_mov_b32_e32 v133, v127
	v_pk_add_f32 v[126:127], v[134:135], v[132:133]
	v_pk_mul_f32 v[132:133], v[88:89], v[88:89]
	v_pk_mul_f32 v[134:135], v[128:129], v[128:129]
	v_pk_mul_f32 v[122:123], v[122:123], s[16:17] op_sel_hi:[1,0]
	v_pk_mov_b32 v[136:137], v[134:135], v[132:133] op_sel:[1,0]
	v_mov_b32_e32 v135, v133
	v_pk_add_f32 v[132:133], v[136:137], v[134:135]
	v_mul_f32_e32 v134, v122, v122
	v_mul_f32_e32 v135, v123, v123
	v_pk_add_f32 v[126:127], v[126:127], v[126:127] op_sel:[0,1] op_sel_hi:[1,0]
	v_pk_add_f32 v[132:133], v[132:133], v[132:133] op_sel:[0,1] op_sel_hi:[1,0]
	v_pk_mul_f32 v[92:93], v[92:93], s[16:17] op_sel_hi:[1,0]
	v_mov_b32_e32 v127, v134
	v_mov_b32_e32 v133, v135
	v_pk_mul_f32 v[96:97], v[96:97], s[16:17] op_sel_hi:[1,0]
	v_pk_add_f32 v[126:127], v[126:127], v[132:133]
	v_mul_f32_e32 v132, v125, v125
	v_mul_f32_e32 v134, v93, v93
	v_mul_f32_e32 v136, v96, v96
	v_mul_f32_e32 v137, v97, v97
	v_pk_fma_f32 v[132:133], v[124:125], v[124:125], v[132:133] op_sel_hi:[1,1,0]
	v_pk_fma_f32 v[134:135], v[92:93], v[92:93], v[134:135] op_sel_hi:[1,1,0]
	v_mov_b32_e32 v133, v136
	v_mov_b32_e32 v135, v137
	v_pk_add_f32 v[132:133], v[132:133], v[134:135]
	v_lshlrev_b32_e32 v194, 16, v82
	v_pk_add_f32 v[126:127], v[126:127], v[132:133]
	v_and_b32_e32 v195, 0xffff0000, v82
	v_add_f32_e32 v126, v126, v127
	v_mov_b32_e32 v127, v1
	v_lshlrev_b32_e32 v82, 16, v83
	v_add_f32_dpp v126, v126, v126 row_shr:1 row_mask:0xf bank_mask:0xf bound_ctrl:1
	v_and_b32_e32 v83, 0xffff0000, v83
	s_mov_b64 s[2:3], -1
	v_add_f32_dpp v126, v126, v126 row_shr:2 row_mask:0xf bank_mask:0xf bound_ctrl:1
	s_nop 1
	v_add_f32_dpp v126, v126, v126 row_shr:4 row_mask:0xf bank_mask:0xf bound_ctrl:1
	s_nop 1
	v_add_f32_dpp v126, v126, v126 row_shr:8 row_mask:0xf bank_mask:0xf bound_ctrl:1
	s_nop 1
	v_mov_b32_dpp v127, v126 row_bcast:15 row_mask:0xa bank_mask:0xf
	v_add_f32_e32 v126, v126, v127
	v_mov_b32_e32 v127, v1
	s_nop 1
	v_mov_b32_dpp v127, v126 row_bcast:31 row_mask:0xc bank_mask:0xf
	v_add_f32_e32 v126, v126, v127
	v_mov_b32_e32 v127, 0x3a800000
	v_readlane_b32 s0, v126, 63
	v_mov_b32_e32 v126, 0x358637bd
	s_nop 0
	v_fma_f32 v126, s0, v127, v126
	v_mul_f32_e32 v127, 0x4b800000, v126
	v_cmp_gt_f32_e32 vcc, s51, v126
	v_readlane_b32 s0, v253, 23
	v_readlane_b32 s1, v253, 24
	v_cndmask_b32_e32 v126, v126, v127, vcc
	v_rsq_f32_e32 v126, v126
	s_nop 0
	v_mul_f32_e32 v127, 0x45800000, v126
	v_cndmask_b32_e32 v126, v126, v127, vcc
	v_pk_mul_f32 v[84:85], v[84:85], v[126:127] op_sel_hi:[1,0]
	v_pk_mul_f32 v[130:131], v[130:131], v[126:127] op_sel_hi:[1,0]
	v_pk_mul_f32 v[84:85], v[76:77], v[84:85]
	v_pk_mul_f32 v[130:131], v[74:75], v[130:131]
	v_pk_fma_f32 v[84:85], v[80:81], v[84:85], v[82:83]
	v_pk_fma_f32 v[82:83], v[78:79], v[130:131], v[194:195]
	s_and_b64 vcc, exec, s[0:1]
	s_cbranch_vccz .LBB0_1404
	v_add_co_u32_e32 v130, vcc, 0xfffff000, v108
	s_mov_b64 s[2:3], 0
	s_nop 0
	v_addc_co_u32_e32 v131, vcc, -1, v109, vcc
	global_store_dwordx4 v[130:131], v[82:85], off offset:-3072 nt
; DI unsigned pk2(float lo, float hi) { f32x2 v = {lo, hi}; bf16x2v r = __builtin_convertvector(v, bf16x2v); return __builtin_bit_cast(unsigned, r); }
; DI void phase_n2(Frame& F, int l) {
;     ...
;             for (int j = 0; j < 4; ++j) { const int o = 4 * F.lane + 256 * j; const f32x4 gv = gpf[j], gt = gtf[j];
;                 xv[j] = xv[j] + gt * (yv[j] * rstd_y * gv);
;                 if (l + 1 < DEPTH) { u32x2 w; w.x = pk2(xv[j][0], xv[j][1]); w.y = pk2(xv[j][2], xv[j][3]); *(u32x2*)(xb + (size_t)r * D + o) = w; } else *(f32x4*)(F.out + (size_t)r * D + o) = xv[j]; }
.LBB0_1404:
	s_andn2_b64 vcc, exec, s[2:3]
	s_cbranch_vccnz .LBB0_1406
	s_mov_b64 s[0:1], 0x63a00000
	v_lshl_add_u64 v[130:131], v[112:113], 0, s[0:1]
	v_cvt_pk_bf16_f32 v132, v82, v83
	v_cvt_pk_bf16_f32 v133, v84, v85
	global_store_dwordx2 v[130:131], v[132:133], off nt
.LBB0_1406:
	v_mov_b32_e32 v127, v126
	v_mov_b32_e32 v132, v126
	v_mov_b32_e32 v133, v126
	v_pk_mul_f32 v[88:89], v[88:89], v[132:133]
	v_pk_mul_f32 v[128:129], v[128:129], v[126:127]
	v_readlane_b32 s0, v253, 23
	v_lshlrev_b32_e32 v130, 16, v86
	v_and_b32_e32 v131, 0xffff0000, v86
	v_lshlrev_b32_e32 v86, 16, v87
	v_and_b32_e32 v87, 0xffff0000, v87
	v_pk_mul_f32 v[88:89], v[72:73], v[88:89]
	v_pk_mul_f32 v[128:129], v[70:71], v[128:129]
	v_readlane_b32 s1, v253, 24
	v_pk_fma_f32 v[88:89], v[68:69], v[88:89], v[86:87]
	v_pk_fma_f32 v[86:87], v[66:67], v[128:129], v[130:131]
	v_cndmask_b32_e64 v128, 0, 1, s[0:1]
	v_cmp_ne_u32_e64 s[6:7], 1, v128
	s_andn2_b64 vcc, exec, s[0:1]
	s_mov_b64 s[2:3], -1
	s_cbranch_vccnz .LBB0_1408
	v_add_co_u32_e32 v128, vcc, 0xfffff000, v108
	s_mov_b64 s[2:3], 0
	s_nop 0
	v_addc_co_u32_e32 v129, vcc, -1, v109, vcc
	global_store_dwordx4 v[128:129], v[86:89], off offset:-2048 nt
.LBB0_1408:
	s_andn2_b64 vcc, exec, s[2:3]
	s_cbranch_vccnz .LBB0_1410
	s_mov_b64 s[0:1], 0x63a00200
	v_lshl_add_u64 v[128:129], v[112:113], 0, s[0:1]
	v_cvt_pk_bf16_f32 v130, v86, v87
	v_cvt_pk_bf16_f32 v131, v88, v89
	global_store_dwordx2 v[128:129], v[130:131], off nt
.LBB0_1410:
	v_mov_b32_e32 v130, v126
	v_mov_b32_e32 v131, v126
	v_pk_mul_f32 v[92:93], v[92:93], v[130:131]
	v_pk_mul_f32 v[124:125], v[124:125], v[126:127]
	v_lshlrev_b32_e32 v128, 16, v90
	v_and_b32_e32 v129, 0xffff0000, v90
	v_lshlrev_b32_e32 v90, 16, v91
	v_and_b32_e32 v91, 0xffff0000, v91
	v_pk_mul_f32 v[92:93], v[64:65], v[92:93]
	v_pk_mul_f32 v[124:125], v[62:63], v[124:125]
	v_pk_fma_f32 v[92:93], v[60:61], v[92:93], v[90:91]
	v_pk_fma_f32 v[90:91], v[58:59], v[124:125], v[128:129]
	s_and_b64 vcc, exec, s[6:7]
	s_mov_b64 s[2:3], -1
	s_cbranch_vccnz .LBB0_1412
	v_add_co_u32_e32 v124, vcc, 0xfffff000, v108
	s_mov_b64 s[2:3], 0
	s_nop 0
	v_addc_co_u32_e32 v125, vcc, -1, v109, vcc
	global_store_dwordx4 v[124:125], v[90:93], off offset:-1024 nt
.LBB0_1412:
	s_andn2_b64 vcc, exec, s[2:3]
	s_cbranch_vccnz .LBB0_1414
	s_mov_b64 s[0:1], 0x63a00400
	v_lshl_add_u64 v[124:125], v[112:113], 0, s[0:1]
	v_cvt_pk_bf16_f32 v128, v90, v91
	v_cvt_pk_bf16_f32 v129, v92, v93
	global_store_dwordx2 v[124:125], v[128:129], off nt
.LBB0_1414:
	v_mov_b32_e32 v128, v126
	v_mov_b32_e32 v129, v126
	v_pk_mul_f32 v[96:97], v[96:97], v[128:129]
	v_pk_mul_f32 v[122:123], v[122:123], v[126:127]
	v_lshlrev_b32_e32 v124, 16, v94
	v_and_b32_e32 v125, 0xffff0000, v94
	v_lshlrev_b32_e32 v94, 16, v95
	v_and_b32_e32 v95, 0xffff0000, v95
	v_pk_mul_f32 v[96:97], v[56:57], v[96:97]
	v_pk_mul_f32 v[122:123], v[54:55], v[122:123]
	v_pk_fma_f32 v[96:97], v[52:53], v[96:97], v[94:95]
	v_pk_fma_f32 v[94:95], v[50:51], v[122:123], v[124:125]
	s_and_b64 vcc, exec, s[6:7]
	s_mov_b64 s[2:3], -1
	s_cbranch_vccnz .LBB0_1416
	s_mov_b64 s[2:3], 0
	global_store_dwordx4 v[108:109], v[94:97], off offset:-4096 nt
.LBB0_1416:
	s_andn2_b64 vcc, exec, s[2:3]
	s_cbranch_vccnz .LBB0_1418
	s_mov_b64 s[0:1], 0x63a00600
	v_lshl_add_u64 v[122:123], v[112:113], 0, s[0:1]
	v_cvt_pk_bf16_f32 v124, v94, v95
	v_cvt_pk_bf16_f32 v125, v96, v97
	global_store_dwordx2 v[122:123], v[124:125], off nt

; DI unsigned pk2(float lo, float hi) { f32x2 v = {lo, hi}; bf16x2v r = __builtin_convertvector(v, bf16x2v); return __builtin_bit_cast(unsigned, r); }
; #define DPP_ADD_(ctrl, rmask, bc) v += __int_as_float(__builtin_amdgcn_update_dpp(0, __float_as_int(v), ctrl, rmask, 0xf, bc))
; DI float wave_sum_dpp(float v) {
;     ...
;     DPP_ADD_(0x111, 0xf, true); DPP_ADD_(0x112, 0xf, true); DPP_ADD_(0x114, 0xf, true); DPP_ADD_(0x118, 0xf, true);
;     DPP_ADD_(0x142, 0xa, false); DPP_ADD_(0x143, 0xc, false);
;     ...
;     return __int_as_float(__builtin_amdgcn_readlane(__float_as_int(v), 63)); }
; #pragma unroll
;     for (int j = 0; j < 4; ++j) s += (v[j][0] * v[j][0] + v[j][1] * v[j][1]) + (v[j][2] * v[j][2] + v[j][3] * v[j][3]);
;     return wave_sum_dpp(s); }
; DI void phase_n2(Frame& F, int l) {
;     ...
;         for (int rr = 0; rr < 2; ++rr) { const int r = r0 + rr;
;             f32x4 yv[4], hv[4]; f32x4 (&xv)[4] = xa[rr];
; #pragma unroll
;             for (int j = 0; j < 4; ++j) yv[j] = ((ya[rr][0][j] + ya[rr][1][j]) + (ya[rr][2][j] + ya[rr][3][j])) * (1.0f / YS8_SCALE);
;             const float rstd_y = rsqrtf(sumsq(yv, F.lane) * (1.0f / D) + RMS_EPS);
; #pragma unroll
;             for (int j = 0; j < 4; ++j) { const int o = 4 * F.lane + 256 * j; const f32x4 gv = gpf[j], gt = gtf[j];
;                 xv[j] = xv[j] + gt * (yv[j] * rstd_y * gv);
;                 if (l + 1 < DEPTH) { u32x2 w; w.x = pk2(xv[j][0], xv[j][1]); w.y = pk2(xv[j][2], xv[j][3]); *(u32x2*)(xb + (size_t)r * D + o) = w; } else *(f32x4*)(F.out + (size_t)r * D + o) = xv[j]; }
.LBB0_1420:
	v_cvt_pk_f32_fp8_e32 v[82:83], v152
	v_cvt_pk_f32_fp8_e32 v[92:93], v148
	v_cvt_pk_f32_fp8_e32 v[162:163], v144
	v_cvt_pk_f32_fp8_e32 v[174:175], v140
	v_cvt_pk_f32_fp8_sdwa v[84:85], v152 src0_sel:WORD_1
	v_cvt_pk_f32_fp8_sdwa v[94:95], v148 src0_sel:WORD_1
	v_cvt_pk_f32_fp8_e32 v[158:159], v145
	v_cvt_pk_f32_fp8_sdwa v[160:161], v145 src0_sel:WORD_1
	v_cvt_pk_f32_fp8_sdwa v[144:145], v144 src0_sel:WORD_1
	v_cvt_pk_f32_fp8_e32 v[170:171], v141
	v_cvt_pk_f32_fp8_sdwa v[172:173], v141 src0_sel:WORD_1
	v_cvt_pk_f32_fp8_sdwa v[140:141], v140 src0_sel:WORD_1
	v_cvt_pk_f32_fp8_e32 v[86:87], v151
	v_cvt_pk_f32_fp8_sdwa v[88:89], v151 src0_sel:WORD_1
	v_cvt_pk_f32_fp8_e32 v[90:91], v150
	v_cvt_pk_f32_fp8_sdwa v[96:97], v150 src0_sel:WORD_1
	v_cvt_pk_f32_fp8_e32 v[150:151], v149
	v_cvt_pk_f32_fp8_sdwa v[152:153], v149 src0_sel:WORD_1
	v_cvt_pk_f32_fp8_e32 v[148:149], v147
	v_cvt_pk_f32_fp8_e32 v[164:165], v143
	v_cvt_pk_f32_fp8_e32 v[176:177], v139
	v_cvt_pk_f32_fp8_sdwa v[154:155], v147 src0_sel:WORD_1
	v_cvt_pk_f32_fp8_sdwa v[166:167], v143 src0_sel:WORD_1
	v_cvt_pk_f32_fp8_sdwa v[178:179], v139 src0_sel:WORD_1
	v_cvt_pk_f32_fp8_e32 v[156:157], v146
	v_cvt_pk_f32_fp8_e32 v[168:169], v142
	v_cvt_pk_f32_fp8_e32 v[180:181], v138
	v_pk_add_f32 v[82:83], v[82:83], v[92:93]
	v_pk_add_f32 v[92:93], v[162:163], v[174:175]
	v_cvt_pk_f32_fp8_sdwa v[146:147], v146 src0_sel:WORD_1
	v_cvt_pk_f32_fp8_sdwa v[142:143], v142 src0_sel:WORD_1
	v_cvt_pk_f32_fp8_sdwa v[138:139], v138 src0_sel:WORD_1
	v_pk_add_f32 v[84:85], v[84:85], v[94:95]
	v_pk_add_f32 v[94:95], v[144:145], v[140:141]
	v_pk_add_f32 v[82:83], v[82:83], v[92:93]
	v_cvt_pk_f32_fp8_e32 v[182:183], v0
	v_pk_add_f32 v[84:85], v[84:85], v[94:95]
	v_pk_mul_f32 v[140:141], v[82:83], s[16:17] op_sel_hi:[1,0]
	v_pk_add_f32 v[82:83], v[86:87], v[148:149]
	v_pk_add_f32 v[86:87], v[164:165], v[176:177]
	v_cvt_pk_f32_fp8_sdwa v[184:185], v0 src0_sel:WORD_1
	v_pk_mul_f32 v[144:145], v[84:85], s[16:17] op_sel_hi:[1,0]
	v_pk_add_f32 v[84:85], v[88:89], v[154:155]
	v_pk_add_f32 v[88:89], v[166:167], v[178:179]
	v_pk_add_f32 v[82:83], v[82:83], v[86:87]
	v_pk_add_f32 v[84:85], v[84:85], v[88:89]
	v_pk_mul_f32 v[94:95], v[82:83], s[16:17] op_sel_hi:[1,0]
	v_pk_add_f32 v[82:83], v[90:91], v[156:157]
	v_pk_add_f32 v[86:87], v[168:169], v[180:181]
	v_pk_mul_f32 v[92:93], v[84:85], s[16:17] op_sel_hi:[1,0]
	v_pk_add_f32 v[84:85], v[96:97], v[146:147]
	v_pk_add_f32 v[88:89], v[142:143], v[138:139]
	v_pk_add_f32 v[82:83], v[82:83], v[86:87]
	v_pk_add_f32 v[84:85], v[84:85], v[88:89]
	v_pk_mul_f32 v[88:89], v[82:83], s[16:17] op_sel_hi:[1,0]
	v_pk_add_f32 v[82:83], v[150:151], v[158:159]
	v_pk_add_f32 v[90:91], v[170:171], v[182:183]
	v_pk_mul_f32 v[86:87], v[84:85], s[16:17] op_sel_hi:[1,0]
	v_pk_add_f32 v[84:85], v[152:153], v[160:161]
	v_pk_add_f32 v[96:97], v[172:173], v[184:185]
	v_pk_add_f32 v[90:91], v[82:83], v[90:91]
	v_pk_add_f32 v[82:83], v[84:85], v[96:97]
	v_pk_mul_f32 v[84:85], v[90:91], s[16:17] op_sel_hi:[1,0]
	v_pk_mul_f32 v[90:91], v[144:145], v[144:145]
	v_pk_mul_f32 v[96:97], v[140:141], v[140:141]
	v_mul_f32_e32 v0, v84, v84
	v_pk_mov_b32 v[138:139], v[96:97], v[90:91] op_sel:[1,0]
	v_mov_b32_e32 v97, v91
	v_pk_add_f32 v[90:91], v[138:139], v[96:97]
	v_pk_mul_f32 v[96:97], v[92:93], v[92:93]
	v_pk_mul_f32 v[138:139], v[94:95], v[94:95]
	v_pk_add_f32 v[90:91], v[90:91], v[90:91] op_sel:[0,1] op_sel_hi:[1,0]
	v_pk_mov_b32 v[142:143], v[138:139], v[96:97] op_sel:[1,0]
	v_mov_b32_e32 v139, v97
	v_pk_add_f32 v[96:97], v[142:143], v[138:139]
	v_mul_f32_e32 v138, v85, v85
	v_pk_add_f32 v[96:97], v[96:97], v[96:97] op_sel:[0,1] op_sel_hi:[1,0]
	v_pk_mul_f32 v[82:83], v[82:83], s[16:17] op_sel_hi:[1,0]
	v_mov_b32_e32 v91, v0
	v_mov_b32_e32 v97, v138
	v_mul_f32_e32 v0, v89, v89
	v_mul_f32_e32 v139, v82, v82
	v_pk_add_f32 v[90:91], v[90:91], v[96:97]
	v_pk_fma_f32 v[96:97], v[88:89], v[88:89], v[0:1] op_sel_hi:[1,1,0]
	v_mul_f32_e32 v0, v87, v87
	v_mul_f32_e32 v142, v83, v83
	v_mov_b32_e32 v97, v139
	v_pk_fma_f32 v[138:139], v[86:87], v[86:87], v[0:1] op_sel_hi:[1,1,0]
	v_lshlrev_b32_e32 v186, 16, v120
	v_mov_b32_e32 v139, v142
	v_pk_add_f32 v[96:97], v[96:97], v[138:139]
	v_and_b32_e32 v187, 0xffff0000, v120
	v_pk_add_f32 v[90:91], v[90:91], v[96:97]
	v_lshlrev_b32_e32 v96, 16, v121
	v_add_f32_e32 v0, v90, v91
	v_mov_b32_e32 v90, v1
	v_and_b32_e32 v97, 0xffff0000, v121
	v_add_f32_dpp v0, v0, v0 row_shr:1 row_mask:0xf bank_mask:0xf bound_ctrl:1
	s_mov_b64 s[2:3], -1
	s_nop 0
	v_add_f32_dpp v0, v0, v0 row_shr:2 row_mask:0xf bank_mask:0xf bound_ctrl:1
	s_nop 1
	v_add_f32_dpp v0, v0, v0 row_shr:4 row_mask:0xf bank_mask:0xf bound_ctrl:1
	s_nop 1
	v_add_f32_dpp v0, v0, v0 row_shr:8 row_mask:0xf bank_mask:0xf bound_ctrl:1
	s_nop 1
	v_mov_b32_dpp v90, v0 row_bcast:15 row_mask:0xa bank_mask:0xf
	v_add_f32_e32 v0, v0, v90
	v_mov_b32_e32 v90, v1
	s_nop 1
	v_mov_b32_dpp v90, v0 row_bcast:31 row_mask:0xc bank_mask:0xf
	v_add_f32_e32 v0, v0, v90
	v_mov_b32_e32 v90, 0x3a800000
	v_readlane_b32 s0, v0, 63
	v_mov_b32_e32 v0, 0x358637bd
	s_nop 0
	v_fma_f32 v0, s0, v90, v0
	v_mul_f32_e32 v90, 0x4b800000, v0
	v_cmp_gt_f32_e32 vcc, s51, v0
	s_nop 1
	v_cndmask_b32_e32 v0, v0, v90, vcc
	v_rsq_f32_e32 v0, v0
	s_nop 0
	v_mul_f32_e32 v90, 0x45800000, v0
	v_cndmask_b32_e32 v90, v0, v90, vcc
	v_pk_mul_f32 v[120:121], v[144:145], v[90:91] op_sel_hi:[1,0]
	v_pk_mul_f32 v[138:139], v[140:141], v[90:91] op_sel_hi:[1,0]
	v_pk_mul_f32 v[76:77], v[76:77], v[120:121]
	v_pk_mul_f32 v[74:75], v[74:75], v[138:139]
	v_pk_fma_f32 v[76:77], v[80:81], v[76:77], v[96:97]
	v_pk_fma_f32 v[74:75], v[78:79], v[74:75], v[186:187]
	s_and_b64 vcc, exec, s[6:7]
	s_cbranch_vccnz .LBB0_1422
	s_mov_b64 s[2:3], 0
	global_store_dwordx4 v[108:109], v[74:77], off offset:-3072 nt
; DI unsigned pk2(float lo, float hi) { f32x2 v = {lo, hi}; bf16x2v r = __builtin_convertvector(v, bf16x2v); return __builtin_bit_cast(unsigned, r); }
; DI void phase_n2(Frame& F, int l) {
;     ...
;             for (int j = 0; j < 4; ++j) { const int o = 4 * F.lane + 256 * j; const f32x4 gv = gpf[j], gt = gtf[j];
;                 xv[j] = xv[j] + gt * (yv[j] * rstd_y * gv);
;                 if (l + 1 < DEPTH) { u32x2 w; w.x = pk2(xv[j][0], xv[j][1]); w.y = pk2(xv[j][2], xv[j][3]); *(u32x2*)(xb + (size_t)r * D + o) = w; } else *(f32x4*)(F.out + (size_t)r * D + o) = xv[j]; }
.LBB0_1422:
	s_andn2_b64 vcc, exec, s[2:3]
	s_cbranch_vccnz .LBB0_1424
	s_mov_b64 s[0:1], 0x63a00800
	v_lshl_add_u64 v[78:79], v[112:113], 0, s[0:1]
	v_cvt_pk_bf16_f32 v80, v74, v75
	v_cvt_pk_bf16_f32 v81, v76, v77
	global_store_dwordx2 v[78:79], v[80:81], off nt
.LBB0_1424:
	v_mov_b32_e32 v91, v90
	v_mov_b32_e32 v96, v90
	v_mov_b32_e32 v97, v90
	v_pk_mul_f32 v[92:93], v[92:93], v[96:97]
	v_pk_mul_f32 v[94:95], v[94:95], v[90:91]
	v_lshlrev_b32_e32 v78, 16, v118
	v_and_b32_e32 v79, 0xffff0000, v118
	v_lshlrev_b32_e32 v80, 16, v119
	v_and_b32_e32 v81, 0xffff0000, v119
	v_pk_mul_f32 v[72:73], v[72:73], v[92:93]
	v_pk_mul_f32 v[70:71], v[70:71], v[94:95]
	v_pk_fma_f32 v[68:69], v[68:69], v[72:73], v[80:81]
	v_pk_fma_f32 v[66:67], v[66:67], v[70:71], v[78:79]
	s_and_b64 vcc, exec, s[6:7]
	s_mov_b64 s[2:3], -1
	s_cbranch_vccnz .LBB0_1426
	s_mov_b64 s[2:3], 0
	global_store_dwordx4 v[108:109], v[66:69], off offset:-2048 nt
.LBB0_1426:
	s_andn2_b64 vcc, exec, s[2:3]
	s_cbranch_vccnz .LBB0_1428
	s_mov_b64 s[0:1], 0x63a00a00
	v_lshl_add_u64 v[70:71], v[112:113], 0, s[0:1]
	v_cvt_pk_bf16_f32 v72, v66, v67
	v_cvt_pk_bf16_f32 v73, v68, v69
	global_store_dwordx2 v[70:71], v[72:73], off nt
.LBB0_1428:
	v_mov_b32_e32 v78, v90
	v_mov_b32_e32 v79, v90
	v_pk_mul_f32 v[78:79], v[86:87], v[78:79]
	v_pk_mul_f32 v[80:81], v[88:89], v[90:91]
	v_lshlrev_b32_e32 v70, 16, v116
	v_and_b32_e32 v71, 0xffff0000, v116
	v_lshlrev_b32_e32 v72, 16, v117
	v_and_b32_e32 v73, 0xffff0000, v117
	v_pk_mul_f32 v[64:65], v[64:65], v[78:79]
	v_pk_mul_f32 v[62:63], v[62:63], v[80:81]
	v_pk_fma_f32 v[60:61], v[60:61], v[64:65], v[72:73]
	v_pk_fma_f32 v[58:59], v[58:59], v[62:63], v[70:71]
	s_and_b64 vcc, exec, s[6:7]
	s_mov_b64 s[2:3], -1
	s_cbranch_vccnz .LBB0_1430
	s_mov_b64 s[2:3], 0
	global_store_dwordx4 v[108:109], v[58:61], off offset:-1024 nt
.LBB0_1430:
	s_andn2_b64 vcc, exec, s[2:3]
	s_cbranch_vccnz .LBB0_1432
	s_mov_b64 s[0:1], 0x63a00c00
	v_lshl_add_u64 v[62:63], v[112:113], 0, s[0:1]
	v_cvt_pk_bf16_f32 v64, v58, v59
	v_cvt_pk_bf16_f32 v65, v60, v61
	global_store_dwordx2 v[62:63], v[64:65], off nt
.LBB0_1432:
	v_mov_b32_e32 v70, v90
	v_mov_b32_e32 v71, v90
	v_pk_mul_f32 v[70:71], v[82:83], v[70:71]
	v_pk_mul_f32 v[72:73], v[84:85], v[90:91]
	v_lshlrev_b32_e32 v62, 16, v114
	v_and_b32_e32 v63, 0xffff0000, v114
	v_lshlrev_b32_e32 v64, 16, v115
	v_and_b32_e32 v65, 0xffff0000, v115
	v_pk_mul_f32 v[56:57], v[56:57], v[70:71]
	v_pk_mul_f32 v[54:55], v[54:55], v[72:73]
	v_pk_fma_f32 v[52:53], v[52:53], v[56:57], v[64:65]
	v_pk_fma_f32 v[50:51], v[50:51], v[54:55], v[62:63]
	s_and_b64 vcc, exec, s[6:7]
	s_mov_b64 s[2:3], -1
	s_cbranch_vccnz .LBB0_1435
	global_store_dwordx4 v[108:109], v[50:53], off nt
	s_cbranch_execz .LBB0_1436

; DI unsigned pk2(float lo, float hi) { f32x2 v = {lo, hi}; bf16x2v r = __builtin_convertvector(v, bf16x2v); return __builtin_bit_cast(unsigned, r); }
; DI void phase_n2(Frame& F, int l) {
;     ...
;             for (int j = 0; j < 4; ++j) { const int o = 4 * F.lane + 256 * j; const f32x4 gv = gpf[j], gt = gtf[j];
;                 xv[j] = xv[j] + gt * (yv[j] * rstd_y * gv);
;                 if (l + 1 < DEPTH) { u32x2 w; w.x = pk2(xv[j][0], xv[j][1]); w.y = pk2(xv[j][2], xv[j][3]); *(u32x2*)(xb + (size_t)r * D + o) = w; } else *(f32x4*)(F.out + (size_t)r * D + o) = xv[j]; }
;             if (l + 1 < DEPTH) { const float rstd_x = rsqrtf(sumsq(xv, F.lane) * (1.0f / D) + RMS_EPS);
;                 mod_norm_store8(xv, rstd_x, mp, F.ws + WS_HF8 + (size_t)r * D, F.lane, hv); } }
;     }
.LBB0_1436:
	s_mov_b64 s[0:1], 0x63a00e00
	v_lshl_add_u64 v[54:55], v[112:113], 0, s[0:1]
	v_cvt_pk_bf16_f32 v56, v50, v51
	v_cvt_pk_bf16_f32 v57, v52, v53
	global_store_dwordx2 v[54:55], v[56:57], off nt
	s_and_b64 vcc, exec, s[4:5]
	s_cbranch_vccnz .LBB0_1399
